# previous best with the out-projection epilogue's 32 residual (x) loads marked non-temporal so that X1 stays in the Infinity Cache for the router phase
# baseline (speedup 1.0000x reference)
.LBB0_1674:
	v_mov_b32_e32 v140, v214
	v_mov_b32_e32 v128, v216
	s_ashr_i32 s44, s69, 11
	s_mul_hi_i32 s45, s44, 0xc000
	v_add_u32_e32 v194, s16, v128
	s_mul_i32 s44, s44, 0xc000
	s_add_u32 s44, s26, s44
	v_ashrrev_i32_e32 v195, 31, v194
	s_addc_u32 s45, s27, s45
	v_lshlrev_b64 v[240:241], 2, v[194:195]
	v_add_u32_e32 v196, s69, v140
	v_lshl_add_u64 v[132:133], s[44:45], 0, v[240:241]
	v_ashrrev_i32_e32 v197, 31, v196
	v_lshl_add_u64 v[134:135], v[132:133], 0, s[22:23]
	v_add_co_u32_e32 v132, vcc, s65, v132
	v_lshl_add_u64 v[198:199], s[10:11], 0, v[240:241]
	v_lshlrev_b64 v[242:243], 13, v[196:197]
	v_lshl_add_u64 v[144:145], v[198:199], 0, v[242:243]
	v_addc_co_u32_e32 v133, vcc, 0, v133, vcc
	global_load_dwordx4 v[136:139], v[134:135], off offset:64
	global_load_dwordx4 v[128:131], v[134:135], off offset:512
	global_load_dwordx4 v[224:227], v[144:145], off nt
	global_load_dwordx4 v[228:231], v[144:145], off offset:64 nt
	global_load_dwordx4 v[232:235], v[144:145], off offset:512 nt
	global_load_dwordx4 v[140:143], v[132:133], off
	s_nop 0
	global_load_dwordx4 v[132:135], v[134:135], off offset:576
	s_nop 0
	global_load_dwordx4 v[236:239], v[144:145], off offset:576 nt
	v_add_u32_e32 v208, 16, v196
	v_ashrrev_i32_e32 v209, 31, v208
	v_add_u32_e32 v204, 32, v196
	v_lshlrev_b64 v[210:211], 13, v[208:209]
	v_ashrrev_i32_e32 v205, 31, v204
	v_add_u32_e32 v200, 48, v196
	v_lshl_add_u64 v[144:145], v[198:199], 0, v[210:211]
	v_lshlrev_b64 v[206:207], 13, v[204:205]
	v_ashrrev_i32_e32 v201, 31, v200
	global_load_dwordx4 v[188:191], v[144:145], off nt
	global_load_dwordx4 v[184:187], v[144:145], off offset:64 nt
	global_load_dwordx4 v[180:183], v[144:145], off offset:512 nt
	global_load_dwordx4 v[176:179], v[144:145], off offset:576 nt
	v_lshl_add_u64 v[144:145], v[198:199], 0, v[206:207]
	v_lshlrev_b64 v[202:203], 13, v[200:201]
	global_load_dwordx4 v[172:175], v[144:145], off nt
	global_load_dwordx4 v[168:171], v[144:145], off offset:64 nt
	global_load_dwordx4 v[164:167], v[144:145], off offset:512 nt
	global_load_dwordx4 v[160:163], v[144:145], off offset:576 nt
	v_lshl_add_u64 v[144:145], v[198:199], 0, v[202:203]
	global_load_dwordx4 v[156:159], v[144:145], off nt
	global_load_dwordx4 v[152:155], v[144:145], off offset:64 nt
	global_load_dwordx4 v[148:151], v[144:145], off offset:512 nt
	s_nop 0
	global_load_dwordx4 v[144:147], v[144:145], off offset:576 nt
	v_and_b32_e32 v222, 64, v220
	v_xor_b32_e32 v221, 16, v220
	v_add_u32_e32 v222, 64, v222
	v_xor_b32_e32 v223, 32, v220
	v_cmp_lt_i32_e32 vcc, v221, v222
	s_ashr_i32 s16, s16, 6
	s_and_b32 s44, s16, -4
	v_cndmask_b32_e32 v221, v220, v221, vcc
	v_cmp_lt_i32_e32 vcc, v223, v222
	v_lshlrev_b32_e32 v222, 2, v221
	s_ashr_i32 s45, s44, 31
	v_cndmask_b32_e32 v223, v220, v223, vcc
	v_lshlrev_b32_e32 v221, 2, v223
	s_waitcnt vmcnt(0)
	v_pk_fma_f32 v[126:127], v[126:127], v[138:139], v[230:231]
	v_pk_fma_f32 v[124:125], v[124:125], v[136:137], v[228:229]
	v_pk_fma_f32 v[118:119], v[118:119], v[142:143], v[226:227]
	v_pk_fma_f32 v[116:117], v[116:117], v[140:141], v[224:225]
	v_pk_fma_f32 v[122:123], v[122:123], v[130:131], v[234:235]
	v_pk_fma_f32 v[120:121], v[120:121], v[128:129], v[232:233]
	v_mul_f32_e32 v223, v125, v125
	v_mul_f32_e32 v228, v127, v127
	v_pk_fma_f32 v[224:225], v[112:113], v[132:133], v[236:237]
	v_mul_f32_e32 v112, v117, v117
	v_mul_f32_e32 v113, v119, v119
	v_mul_f32_e32 v229, v121, v121
	v_mul_f32_e32 v230, v123, v123
	v_pk_fma_f32 v[226:227], v[114:115], v[134:135], v[238:239]
	v_fmac_f32_e32 v223, v124, v124
	v_fmac_f32_e32 v228, v126, v126
	v_fmac_f32_e32 v112, v116, v116
	v_fmac_f32_e32 v113, v118, v118
	v_fmac_f32_e32 v229, v120, v120
	v_fmac_f32_e32 v230, v122, v122
	v_mul_f32_e32 v114, v225, v225
	v_mul_f32_e32 v115, v227, v227
	v_add_f32_e32 v223, v223, v228
	v_add_f32_e32 v112, v112, v113
	v_add_f32_e32 v228, v229, v230
	v_fmac_f32_e32 v114, v224, v224
	v_add_f32_e32 v112, v112, v223
	v_fmac_f32_e32 v115, v226, v226
	v_add_f32_e32 v112, v112, v228
	v_add_f32_e32 v113, v114, v115
	v_add_f32_e32 v223, v112, v113
	ds_bpermute_b32 v228, v222, v223
	v_lshl_add_u64 v[112:113], s[24:25], 0, v[242:243]
	v_lshl_add_u64 v[114:115], v[112:113], 0, v[240:241]
	global_store_dwordx4 v[114:115], v[116:119], off
	global_store_dwordx4 v[114:115], v[124:127], off offset:64
	global_store_dwordx4 v[114:115], v[120:123], off offset:512
	global_store_dwordx4 v[114:115], v[224:227], off offset:576
	s_waitcnt lgkmcnt(0)
	v_add_f32_e32 v112, v223, v228
	ds_bpermute_b32 v113, v221, v112
	s_and_saveexec_b64 s[46:47], s[6:7]
	s_cbranch_execz .LBB0_1676
	v_lshlrev_b64 v[114:115], 7, v[196:197]
	v_lshl_add_u64 v[114:115], s[14:15], 0, v[114:115]
	v_lshl_add_u64 v[114:115], s[44:45], 2, v[114:115]
	s_lshl_b32 s16, s59, 2
	v_lshl_add_u64 v[114:115], v[114:115], 0, s[16:17]
	s_waitcnt lgkmcnt(0)
	v_add_f32_e32 v112, v112, v113
	global_store_dword v[114:115], v112, off

.LBB0_1682:
	s_or_b64 exec, exec, s[46:47]
	v_add_u32_e32 v124, 0x80, v196
	v_ashrrev_i32_e32 v125, 31, v124
	v_lshlrev_b64 v[126:127], 13, v[124:125]
	s_waitcnt lgkmcnt(0)
	v_lshl_add_u64 v[64:65], v[198:199], 0, v[126:127]
	global_load_dwordx4 v[144:147], v[64:65], off nt
	global_load_dwordx4 v[148:151], v[64:65], off offset:64 nt
	global_load_dwordx4 v[152:155], v[64:65], off offset:512 nt
	global_load_dwordx4 v[156:159], v[64:65], off offset:576 nt
	v_add_u32_e32 v120, 0x90, v196
	v_add_u32_e32 v116, 0xa0, v196
	v_add_u32_e32 v112, 0xb0, v196
	v_ashrrev_i32_e32 v121, 31, v120
	v_ashrrev_i32_e32 v117, 31, v116
	v_ashrrev_i32_e32 v113, 31, v112
	v_lshlrev_b64 v[122:123], 13, v[120:121]
	v_lshlrev_b64 v[118:119], 13, v[116:117]
	v_lshlrev_b64 v[114:115], 13, v[112:113]
	v_lshl_add_u64 v[64:65], v[198:199], 0, v[122:123]
	v_lshl_add_u64 v[66:67], v[198:199], 0, v[118:119]
	v_lshl_add_u64 v[160:161], v[198:199], 0, v[114:115]
	global_load_dwordx4 v[108:111], v[64:65], off nt
	global_load_dwordx4 v[104:107], v[64:65], off offset:64 nt
	global_load_dwordx4 v[100:103], v[64:65], off offset:512 nt
	global_load_dwordx4 v[96:99], v[64:65], off offset:576 nt
	global_load_dwordx4 v[92:95], v[66:67], off nt
	global_load_dwordx4 v[88:91], v[66:67], off offset:64 nt
	global_load_dwordx4 v[84:87], v[66:67], off offset:512 nt
	global_load_dwordx4 v[80:83], v[66:67], off offset:576 nt
	global_load_dwordx4 v[76:79], v[160:161], off nt
	global_load_dwordx4 v[72:75], v[160:161], off offset:64 nt
	global_load_dwordx4 v[68:71], v[160:161], off offset:512 nt
	s_nop 0
	global_load_dwordx4 v[64:67], v[160:161], off offset:576 nt
	s_waitcnt vmcnt(15)
	v_pk_fma_f32 v[62:63], v[62:63], v[142:143], v[146:147]
	v_pk_fma_f32 v[60:61], v[60:61], v[140:141], v[144:145]
	s_waitcnt vmcnt(14)
	v_pk_fma_f32 v[58:59], v[58:59], v[138:139], v[150:151]
	v_pk_fma_f32 v[56:57], v[56:57], v[136:137], v[148:149]
	s_waitcnt vmcnt(13)
	v_pk_fma_f32 v[54:55], v[54:55], v[130:131], v[154:155]
	v_pk_fma_f32 v[52:53], v[52:53], v[128:129], v[152:153]
	s_waitcnt vmcnt(12)
	v_pk_fma_f32 v[146:147], v[50:51], v[134:135], v[158:159]
	v_pk_fma_f32 v[144:145], v[48:49], v[132:133], v[156:157]
	v_mul_f32_e32 v48, v61, v61
	v_mul_f32_e32 v49, v63, v63
	v_mul_f32_e32 v50, v57, v57
	v_mul_f32_e32 v51, v59, v59
	v_mul_f32_e32 v148, v53, v53
	v_mul_f32_e32 v149, v55, v55
	v_fmac_f32_e32 v48, v60, v60
	v_fmac_f32_e32 v49, v62, v62
	v_fmac_f32_e32 v50, v56, v56
	v_fmac_f32_e32 v51, v58, v58
	v_mul_f32_e32 v150, v145, v145
	v_mul_f32_e32 v151, v147, v147
	v_fmac_f32_e32 v148, v52, v52
	v_fmac_f32_e32 v149, v54, v54
	v_add_f32_e32 v48, v48, v49
	v_add_f32_e32 v49, v50, v51
	v_fmac_f32_e32 v150, v144, v144
	v_fmac_f32_e32 v151, v146, v146
	v_add_f32_e32 v50, v148, v149
	v_add_f32_e32 v48, v48, v49
	v_add_f32_e32 v48, v48, v50
	v_add_f32_e32 v49, v150, v151
	v_add_f32_e32 v148, v48, v49
	ds_bpermute_b32 v149, v222, v148
	v_lshl_add_u64 v[48:49], s[24:25], 0, v[126:127]
	v_lshl_add_u64 v[50:51], v[194:195], 2, v[48:49]
	global_store_dwordx4 v[50:51], v[60:63], off
	global_store_dwordx4 v[50:51], v[56:59], off offset:64
	global_store_dwordx4 v[50:51], v[52:55], off offset:512
	global_store_dwordx4 v[50:51], v[144:147], off offset:576
	s_waitcnt lgkmcnt(0)
	v_add_f32_e32 v48, v148, v149
	ds_bpermute_b32 v49, v221, v48
	s_and_saveexec_b64 s[46:47], s[6:7]
	s_cbranch_execz .LBB0_1684
	v_lshlrev_b64 v[50:51], 7, v[124:125]
	v_lshl_add_u64 v[50:51], s[14:15], 0, v[50:51]
	v_lshl_add_u64 v[50:51], s[44:45], 2, v[50:51]
	s_lshl_b32 s16, s59, 2
	v_lshl_add_u64 v[50:51], v[50:51], 0, s[16:17]
	s_waitcnt lgkmcnt(0)
	v_add_f32_e32 v48, v48, v49
	global_store_dword v[50:51], v48, off
